# attention tile loop: static s_setprio 1 for waves 4-7 (reset after the loop), on top of best
# speedup vs baseline: 1.0073x; 1.0073x over previous
; #define LAS __attribute__((address_space(3)))
; __device__ __forceinline__ int opaque_tid() { int t = threadIdx.x; asm volatile("" : "+v"(t)); return t; }
; __device__ __forceinline__ int v_rd_base(int lane) { return ((lane & 3) << 3) | (((lane >> 2) & 3) << 6) | (((lane >> 4) & 1) << 5) | (((lane >> 5) & 1) << 8); }
; __device__ __forceinline__ int v_st256(int k, int c) { const int kk = (k & ~0xC) | ((k & 4) << 1) | ((k & 8) >> 1); return ((kk >> 3) * 8 + (c >> 5)) * 512 + ((kk & 7) * 32 + (c & 31)) * 2; }
; #define SLOAD_A(k0) do { const bf16_t* vp_ = Vh + (long)(k0) * LDK + toff; const bf16_t* kp_ = Kh + (long)(k0) * LDK + toff; \
;     sa0 = *(const bf16x8*)kp_; sa1 = *(const bf16x8*)(kp_ + 32L * LDK); sa2 = *(const bf16x8*)vp_; sa3 = *(const bf16x8*)(vp_ + 128); } while (0)
; #define SWRITE_A(b) do { LAS char* vb_ = V_lds + (b) * SHM_V2 + vst00; LAS char* kb_ = K_lds + (b) * SHM_K2 + kst0; \
;     *(LAS bf16x8*)(kb_) = sa0; *(LAS bf16x8*)(kb_ + 8192) = sa1; *(LAS bf16x8*)(vb_) = sa2; *(LAS bf16x8*)(vb_ + 2048) = sa3; } while (0)
; template <int LDQ, int LDK, int LDO>
; __device__ __forceinline__ void attn_body256(const bf16_t* __restrict__ Qb, const bf16_t* __restrict__ Kh, const bf16_t* __restrict__ Vh, float* __restrict__ Ob, int seq, LAS char* lds) {
;   const int tid = opaque_tid(), wid = tid >> 6, lane = tid & 63, r32 = lane & 31, hi = lane >> 5;
;   LAS char* V_lds = lds; LAS char* K_lds = lds + 2 * SHM_V2;
;   LAS float* wsl = (LAS float*)(lds + 2 * SHM_V2 + 2 * SHM_K2) + wid * 64; LAS float* li_l = wsl; LAS float* al_l = wsl + 32;
;   float m_reg = -1e30f, l_reg = 0; f32x16 o[8] = {}; bf16x8 qr[8];
;   const bf16_t* Qw = Qb + (long)(wid * QBLK + r32) * LDQ + hi * 8;
; #pragma unroll
;   for (int d0 = 0; d0 < 8; ++d0) qr[d0] = *(const bf16x8*)(Qw + d0 * 16);
;   const int sr = tid >> 4, sc = (tid & 15) * 8;
;   const int vst00 = v_st256(sr, sc), kst0 = KSWZ(sr, sc * 2);
;   const unsigned toff = (unsigned)(sr * LDK + sc);
;   const int vb0 = (int)(uintptr_t)V_lds + v_rd_base(lane);
;   bf16x8 sa0, sa1, sa2, sa3;
;     ...
;   f32x16 p0, p1; float mn, al; bf16x8 pa0, pa1, pa2, pa3; const int NT = seq / KVBLK;
;   SLOAD_A(0); asm volatile("s_waitcnt vmcnt(0)" ::: "memory"); SWRITE_A(0); SLOAD_B(0); asm volatile("s_waitcnt vmcnt(0)" ::: "memory"); SWRITE_B(0); __syncthreads();
.LBB0_933:
	s_lshl_b64 s[8:9], s[10:11], 1
	s_add_u32 s6, s4, s8
	s_addc_u32 s7, s5, s9
	v_mov_b32_e32 v226, v241
	v_readfirstlane_b32 s89, v241
	s_lshr_b32 s89, s89, 8
	s_cmp_lg_u32 s89, 0
	s_cbranch_scc0 .Lattn_prio_skip
	s_setprio 1
.Lattn_prio_skip:
	s_movk_i32 s82, 0xffe0
	v_ashrrev_i32_e32 v17, 1, v241
	v_bfe_u32 v231, v241, 5, 1
	v_bfi_b32 v2, s82, v17, v241
	v_mov_b64_e32 v[4:5], s[6:7]
	s_movk_i32 s6, 0x3080
	v_mad_i64_i32 v[4:5], s[6:7], v2, s6, v[4:5]
	v_lshlrev_b32_e32 v212, 4, v231
	v_mov_b32_e32 v213, v3
	v_lshlrev_b32_e32 v19, 3, v241
	v_lshl_add_u64 v[4:5], v[4:5], 0, v[212:213]
	v_ashrrev_i32_e32 v18, 4, v241
	v_and_b32_e32 v2, 0x78, v19
	s_movk_i32 s6, 0x1840
	global_load_dwordx4 v[164:167], v[4:5], off
	global_load_dwordx4 v[168:171], v[4:5], off offset:32
	global_load_dwordx4 v[172:175], v[4:5], off offset:64
	global_load_dwordx4 v[176:179], v[4:5], off offset:96
	global_load_dwordx4 v[180:183], v[4:5], off offset:128
	global_load_dwordx4 v[184:187], v[4:5], off offset:160
	global_load_dwordx4 v[188:191], v[4:5], off offset:192
	global_load_dwordx4 v[192:195], v[4:5], off offset:224
	v_mad_u64_u32 v[4:5], s[6:7], v18, s6, v[2:3]
	s_add_u32 s10, s16, s8
	v_mov_b32_e32 v5, v3
	s_addc_u32 s11, s17, s9
	v_lshlrev_b64 v[12:13], 1, v[4:5]
	v_lshl_add_u64 v[4:5], s[10:11], 0, v[12:13]
	s_mov_b32 s6, 0x61000
	s_waitcnt vmcnt(10)
	v_add_co_u32_e32 v8, vcc, s6, v4
	v_lshl_add_u64 v[14:15], s[18:19], 0, v[12:13]
	s_nop 0
	v_addc_co_u32_e32 v9, vcc, 0, v5, vcc
	global_load_dwordx4 v[4:7], v[4:5], off
	s_nop 0
	global_load_dwordx4 v[8:11], v[8:9], off
	s_nop 0
	global_load_dwordx4 v[196:199], v[14:15], off
	global_load_dwordx4 v[200:203], v[14:15], off offset:256
	s_waitcnt vmcnt(0)
	v_lshl_add_u64 v[14:15], s[24:25], 0, v[12:13]
	global_load_dwordx4 v[204:207], v[14:15], off
	global_load_dwordx4 v[208:211], v[14:15], off offset:256
	v_and_b32_e32 v15, 0x3fffffc0, v241
	v_lshlrev_b32_e32 v20, 4, v241
	v_and_b32_e32 v214, 0xffffffe0, v17
	v_lshlrev_b32_e32 v17, 1, v18
	v_lshl_add_u32 v232, v15, 2, s64
	v_and_b32_e32 v15, 3, v18
	v_lshrrev_b32_e32 v22, 1, v18
	v_and_b32_e32 v23, 0x7ffff0, v18
	v_bfe_u32 v24, v19, 5, 2
	v_and_b32_e32 v26, 0x70, v20
	v_and_b32_e32 v17, 8, v17
	v_lshlrev_b32_e32 v2, 1, v2
	s_movk_i32 s7, 0x60
	v_lshlrev_b32_e32 v21, 1, v241
	v_lshlrev_b32_e32 v18, 8, v18
	v_and_b32_e32 v25, 0xc0, v20
	v_and_or_b32 v15, v22, 4, v15
	s_add_i32 s6, 0, 0x10000
	v_bitop3_b32 v215, v212, v20, s65 bitop3:0x78
	v_bitop3_b32 v235, v212, v26, s7 bitop3:0x36
	s_movk_i32 s7, 0x80
	v_or3_b32 v17, v23, v17, v24
	v_and_b32_e32 v20, 48, v2
	v_bitop3_b32 v2, v2, v241, s65 bitop3:0x78
	v_and_b32_e32 v213, 31, v241
	v_and_b32_e32 v21, 32, v21
	v_bitop3_b32 v236, v212, v26, s7 bitop3:0x36
	s_movk_i32 s7, 0xa0
	v_lshlrev_b32_e32 v15, 6, v15
	v_lshl_add_u32 v16, v17, 9, 0
	v_add3_u32 v240, s6, v2, v18
	s_movk_i32 s11, 0x118
	s_add_u32 s8, s78, s8
	v_and_b32_e32 v14, 63, v241
	v_bitop3_b32 v237, v212, v26, s7 bitop3:0x36
	s_movk_i32 s7, 0xc0
	v_lshl_add_u32 v239, v213, 8, s6
	v_add3_u32 v241, v16, v15, v20
	s_movk_i32 s6, 0xe0
	v_and_or_b32 v2, v19, s11, v21
	s_addc_u32 s9, s79, s9
	v_mov_b32_e32 v16, v3
	v_mov_b32_e32 v17, v3
	v_bitop3_b32 v233, v212, v26, 32 bitop3:0x36
	v_bitop3_b32 v234, v212, v26, 64 bitop3:0x36
	v_bitop3_b32 v238, v212, v26, s7 bitop3:0x36
	v_bitop3_b32 v242, v212, v26, s6 bitop3:0x36
	v_cmp_gt_u32_e64 s[6:7], 32, v14
	v_add3_u32 v244, v25, 0, v2
	v_lshl_add_u64 v[216:217], s[78:79], 0, v[12:13]
	v_lshl_add_u64 v[218:219], s[8:9], 0, v[12:13]
	v_mov_b32_e32 v2, v3
	v_mov_b32_e32 v12, v3
	v_mov_b32_e32 v13, v3
	s_waitcnt vmcnt(5)
	ds_write_b128 v240, v[4:7]
	s_waitcnt vmcnt(4)
	ds_write_b128 v240, v[8:11] offset:8192
	s_waitcnt vmcnt(3)
	ds_write_b128 v241, v[196:199]
	s_waitcnt vmcnt(2)
	ds_write_b128 v241, v[200:203] offset:2048
	s_waitcnt vmcnt(0)
	v_mov_b32_e32 v4, v3
	v_mov_b32_e32 v5, v3
	v_mov_b32_e32 v6, v3
	v_mov_b32_e32 v7, v3
	v_mov_b32_e32 v8, v3
	v_mov_b32_e32 v9, v3
	v_mov_b32_e32 v10, v3
	v_mov_b32_e32 v11, v3
	v_mov_b32_e32 v14, v3
	v_mov_b32_e32 v15, v3
	v_mov_b64_e32 v[130:131], v[16:17]
	v_mov_b64_e32 v[114:115], v[16:17]
	v_mov_b64_e32 v[98:99], v[16:17]
	v_mov_b64_e32 v[82:83], v[16:17]
	v_mov_b64_e32 v[66:67], v[16:17]
	v_mov_b64_e32 v[50:51], v[16:17]
	v_mov_b64_e32 v[34:35], v[16:17]
	v_mov_b64_e32 v[128:129], v[14:15]
	v_mov_b64_e32 v[126:127], v[12:13]
	v_mov_b64_e32 v[124:125], v[10:11]
	v_mov_b64_e32 v[122:123], v[8:9]
	v_mov_b64_e32 v[120:121], v[6:7]
	v_mov_b64_e32 v[118:119], v[4:5]
	v_mov_b64_e32 v[116:117], v[2:3]
	v_mov_b64_e32 v[112:113], v[14:15]
	v_mov_b64_e32 v[110:111], v[12:13]
	v_mov_b64_e32 v[108:109], v[10:11]
	v_mov_b64_e32 v[106:107], v[8:9]
	v_mov_b64_e32 v[104:105], v[6:7]
	v_mov_b64_e32 v[102:103], v[4:5]
	v_mov_b64_e32 v[100:101], v[2:3]
	v_mov_b64_e32 v[96:97], v[14:15]
	v_mov_b64_e32 v[94:95], v[12:13]
	v_mov_b64_e32 v[92:93], v[10:11]
	v_mov_b64_e32 v[90:91], v[8:9]
	v_mov_b64_e32 v[88:89], v[6:7]
	v_mov_b64_e32 v[86:87], v[4:5]
	v_mov_b64_e32 v[84:85], v[2:3]
	v_mov_b64_e32 v[80:81], v[14:15]
	v_mov_b64_e32 v[78:79], v[12:13]
	v_mov_b64_e32 v[76:77], v[10:11]
	v_mov_b64_e32 v[74:75], v[8:9]
	v_mov_b64_e32 v[72:73], v[6:7]
	v_mov_b64_e32 v[70:71], v[4:5]
	v_mov_b64_e32 v[68:69], v[2:3]
	v_mov_b64_e32 v[64:65], v[14:15]
	v_mov_b64_e32 v[62:63], v[12:13]
	v_mov_b64_e32 v[60:61], v[10:11]
	v_mov_b64_e32 v[58:59], v[8:9]
	v_mov_b64_e32 v[56:57], v[6:7]
	v_mov_b64_e32 v[54:55], v[4:5]
	v_mov_b64_e32 v[52:53], v[2:3]
	v_mov_b64_e32 v[48:49], v[14:15]
	v_mov_b64_e32 v[46:47], v[12:13]
	v_mov_b64_e32 v[44:45], v[10:11]
	v_mov_b64_e32 v[42:43], v[8:9]
	v_mov_b64_e32 v[40:41], v[6:7]
	v_mov_b64_e32 v[38:39], v[4:5]
	v_mov_b64_e32 v[36:37], v[2:3]
	v_mov_b64_e32 v[32:33], v[14:15]
	v_mov_b64_e32 v[30:31], v[12:13]
	v_mov_b64_e32 v[28:29], v[10:11]
	v_mov_b64_e32 v[26:27], v[8:9]
	v_mov_b64_e32 v[24:25], v[6:7]
	v_mov_b64_e32 v[22:23], v[4:5]
	v_mov_b64_e32 v[20:21], v[2:3]
	v_mov_b64_e32 v[18:19], v[16:17]
	s_mov_b32 s10, 0
	v_lshl_add_u32 v243, v213, 2, v232
	v_mov_b32_e32 v245, 0
	v_mov_b32_e32 v248, 0xf149f2ca
	s_mov_b64 s[82:83], 0
	s_mov_b32 s86, 0x8000
	v_mov_b64_e32 v[16:17], v[14:15]
	v_mov_b64_e32 v[14:15], v[12:13]
	v_mov_b64_e32 v[12:13], v[10:11]
	v_mov_b64_e32 v[10:11], v[8:9]
	v_mov_b64_e32 v[8:9], v[6:7]
	v_mov_b64_e32 v[6:7], v[4:5]
	v_mov_b64_e32 v[4:5], v[2:3]
	s_waitcnt vmcnt(1)
	ds_write_b128 v241, v[204:207] offset:16384
	s_waitcnt vmcnt(0)
	ds_write_b128 v241, v[208:211] offset:18432
	s_waitcnt lgkmcnt(0)
	s_barrier

; template <int LDQ, int LDK, int LDO>
; __device__ __forceinline__ void attn_body256(const bf16_t* __restrict__ Qb, const bf16_t* __restrict__ Kh, const bf16_t* __restrict__ Vh, float* __restrict__ Ob, int seq, LAS char* lds) {
;     ...
;   if (hi == 0) li_l[r32] = l_reg; asm volatile("s_waitcnt lgkmcnt(0)" ::: "memory");
.LBB0_946:
	s_setprio 0
	s_and_saveexec_b64 s[8:9], s[6:7]
	s_cbranch_execz .LBB0_915
	ds_write_b32 v243, v132
	s_branch .LBB0_915
